# attention per-gap DMA variant: MFMA as the M0 wait state (no s_nop), V address setup spread over two gaps (on v11)
# speedup vs baseline: 1.0031x; 1.0031x over previous
.LBB0_1235:
	s_add_i32 s15, s14, 1
	s_cmp_lg_u32 s14, 2
	s_cselect_b32 s14, s15, 0
	s_mul_i32 s15, s14, 0x6400
	v_add_u32_e32 v70, s15, v185
	ds_read_b128 v[66:69], v70
	ds_read_b128 v[166:169], v70 offset:32
	ds_read_b128 v[170:173], v70 offset:64
	ds_read_b128 v[188:191], v70 offset:96
	ds_read_b128 v[192:195], v70 offset:128
	ds_read_b128 v[196:199], v70 offset:160
	ds_read_b128 v[200:203], v70 offset:192
	ds_read_b128 v[216:219], v70 offset:224
	ds_read_b128 v[220:223], v70 offset:256
	ds_read_b128 v[224:227], v70 offset:288
	ds_read_b128 v[228:231], v70 offset:320
	ds_read_b128 v[146:149], v70 offset:352
	s_waitcnt lgkmcnt(11)
	v_mfma_f32_32x32x16_bf16 v[66:81], v[66:69], v[142:145], 0
	v_sub_f32_e32 v82, v82, v183
	v_exp_f32_e32 v82, v82
	v_sub_f32_e32 v94, v94, v183
	v_exp_f32_e32 v94, v94
	v_add_f32_e32 v165, 0, v82
	v_add_f32_e32 v165, v94, v165
	s_waitcnt lgkmcnt(10)
	v_mfma_f32_32x32x16_bf16 v[66:81], v[166:169], v[138:141], v[66:81]
	v_sub_f32_e32 v83, v83, v183
	v_exp_f32_e32 v83, v83
	v_sub_f32_e32 v95, v95, v183
	v_exp_f32_e32 v95, v95
	v_add_f32_e32 v165, v83, v165
	v_cvt_pk_bf16_f32 v82, v82, v83
	v_add_f32_e32 v165, v95, v165
	v_sub_f32_e32 v83, v84, v183
	s_waitcnt lgkmcnt(9)
	v_mfma_f32_32x32x16_bf16 v[66:81], v[170:173], v[134:137], v[66:81]
	v_exp_f32_e32 v83, v83
	v_sub_f32_e32 v96, v96, v183
	v_add_f32_e32 v84, v83, v165
	v_exp_f32_e32 v165, v96
	s_nop 0
	v_add_f32_e32 v84, v165, v84
	s_waitcnt lgkmcnt(8)
	v_mfma_f32_32x32x16_bf16 v[66:81], v[188:191], v[130:133], v[66:81]
	v_sub_f32_e32 v85, v85, v183
	v_exp_f32_e32 v85, v85
	v_sub_f32_e32 v96, v97, v183
	v_exp_f32_e32 v97, v96
	v_cvt_pk_bf16_f32 v96, v94, v95
	v_add_f32_e32 v84, v85, v84
	v_cvt_pk_bf16_f32 v83, v83, v85
	v_add_f32_e32 v84, v97, v84
	v_cvt_pk_bf16_f32 v97, v165, v97
	s_waitcnt lgkmcnt(7)
	v_mfma_f32_32x32x16_bf16 v[66:81], v[192:195], v[126:129], v[66:81]
	v_sub_f32_e32 v85, v86, v183
	v_exp_f32_e32 v85, v85
	s_nop 0
	v_add_f32_e32 v84, v85, v84
	s_waitcnt lgkmcnt(6)
	v_mfma_f32_32x32x16_bf16 v[66:81], v[196:199], v[122:125], v[66:81]
	v_sub_f32_e32 v86, v87, v183
	v_exp_f32_e32 v86, v86
	s_nop 0
	v_add_f32_e32 v87, v86, v84
	v_cvt_pk_bf16_f32 v84, v85, v86
	s_waitcnt lgkmcnt(5)
	v_mfma_f32_32x32x16_bf16 v[66:81], v[200:203], v[118:121], v[66:81]
	v_sub_f32_e32 v85, v88, v183
	v_exp_f32_e32 v85, v85
	s_nop 0
	v_add_f32_e32 v86, v85, v87
	s_waitcnt lgkmcnt(4)
	v_mfma_f32_32x32x16_bf16 v[66:81], v[216:219], v[114:117], v[66:81]
	v_sub_f32_e32 v87, v89, v183
	v_exp_f32_e32 v87, v87
	s_nop 0
	v_add_f32_e32 v86, v87, v86
	v_cvt_pk_bf16_f32 v85, v85, v87
	v_sub_f32_e32 v87, v90, v183
	v_exp_f32_e32 v90, v87
	s_waitcnt lgkmcnt(3)
	v_mfma_f32_32x32x16_bf16 v[66:81], v[220:223], v[110:113], v[66:81]
	v_add_u32_e32 v165, s13, v187
	v_add_f32_e32 v94, v90, v86
	ds_read_b128 v[86:89], v165
	ds_read_b128 v[166:169], v165 offset:32
	s_waitcnt lgkmcnt(4)
	v_mfma_f32_32x32x16_bf16 v[66:81], v[224:227], v[106:109], v[66:81]
	v_sub_f32_e32 v91, v91, v183
	ds_read_b128 v[170:173], v165 offset:4608
	ds_read_b128 v[188:191], v165 offset:4640
	v_exp_f32_e32 v91, v91
	s_nop 0
	v_add_f32_e32 v95, v91, v94
	v_cvt_pk_bf16_f32 v94, v90, v91
	s_waitcnt lgkmcnt(5)
	v_mfma_f32_32x32x16_bf16 v[66:81], v[228:231], v[102:105], v[66:81]
	v_sub_f32_e32 v90, v92, v183
	ds_read_b128 v[192:195], v165 offset:9216
	ds_read_b128 v[196:199], v165 offset:9248
	v_exp_f32_e32 v90, v90
	s_nop 0
	v_add_f32_e32 v91, v90, v95
	v_sub_f32_e32 v92, v93, v183
	v_exp_f32_e32 v92, v92
	s_waitcnt lgkmcnt(6)
	v_mfma_f32_32x32x16_bf16 v[66:81], v[146:149], v[98:101], v[66:81]
	v_add_f32_e32 v186, v92, v91
	v_cvt_pk_bf16_f32 v95, v90, v92
	ds_read_b128 v[90:93], v165 offset:13824
	ds_read_b128 v[146:149], v165 offset:13856
	s_orn2_b64 vcc, s[0:1], s[24:25]
	s_and_b64 vcc, vcc, exec
	s_cbranch_vccnz .LattB_slow
	s_mul_i32 s13, s12, 0x6400
	s_add_u32 s16, s80, s2
	s_addc_u32 s17, s81, s3
	s_add_u32 s16, s16, 0x30e90000
	s_addc_u32 s17, s17, 0
	s_add_i32 m0, s13, s65
	s_waitcnt lgkmcnt(0)
	v_mfma_f32_32x32x16_bf16 v[50:65], v[86:89], v[82:85], v[50:65]
	v_add_f32_e32 v186, v164, v186
	global_load_lds_dwordx4 v208, s[16:17]
	s_add_i32 m0, s13, s66
	v_mfma_f32_32x32x16_bf16 v[34:49], v[170:173], v[82:85], v[34:49]
	global_load_lds_dwordx4 v209, s[16:17]
	s_add_i32 m0, s13, s67
	s_add_i32 s13, s13, s68
	v_mfma_f32_32x32x16_bf16 v[18:33], v[192:195], v[82:85], v[18:33]
	v_max_f32_e32 v150, v66, v67
	v_max3_f32 v150, v150, v68, v69
	global_load_lds_dwordx4 v210, s[16:17]
	s_add_i32 m0, s13, 0x6000
	s_mul_i32 s13, s12, 0x4800
	s_add_i32 s15, s13, 0xffffb800
	s_cmp_lg_u32 s12, 0
	v_mfma_f32_32x32x16_bf16 v[2:17], v[90:93], v[82:85], v[2:17]
	v_max3_f32 v150, v150, v70, v71
	v_max3_f32 v150, v150, v72, v73
	global_load_lds_dwordx4 v211, s[16:17]
	s_cselect_b32 s15, s15, 0x9000
	s_add_i32 s15, s15, 0x12c00
	s_add_u32 s16, s82, s2
	s_addc_u32 s17, s83, s3
	s_add_u32 s16, s16, 0x31bf8180
	s_addc_u32 s17, s17, 0
	s_add_i32 m0, s15, s69
	v_mfma_f32_32x32x16_bf16 v[50:65], v[166:169], v[94:97], v[50:65]
	v_max3_f32 v150, v150, v74, v75
	v_max3_f32 v150, v150, v76, v77
	global_load_lds_dwordx4 v212, s[16:17]
	s_add_i32 m0, s15, s70
	v_mfma_f32_32x32x16_bf16 v[34:49], v[188:191], v[94:97], v[34:49]
	v_max3_f32 v150, v150, v78, v79
	v_max3_f32 v150, v150, v80, v81
	global_load_lds_dwordx4 v213, s[16:17]
	s_add_i32 m0, s15, s71
	v_mfma_f32_32x32x16_bf16 v[18:33], v[196:199], v[94:97], v[18:33]
	global_load_lds_dwordx4 v214, s[16:17]
	v_mfma_f32_32x32x16_bf16 v[2:17], v[146:149], v[94:97], v[2:17]
	v_mov_b32_e32 v151, v150
	s_nop 1
	v_permlane32_swap_b32_e32 v151, v150
	v_max_f32_e32 v150, v150, v151
	s_branch .LattB_join

.LBB0_1240:
	s_mul_i32 s13, s14, 0x6400
	v_add_u32_e32 v86, s13, v185
	ds_read_b128 v[82:85], v86
	ds_read_b128 v[188:191], v86 offset:32
	ds_read_b128 v[192:195], v86 offset:64
	ds_read_b128 v[196:199], v86 offset:96
	ds_read_b128 v[200:203], v86 offset:128
	ds_read_b128 v[216:219], v86 offset:160
	ds_read_b128 v[220:223], v86 offset:192
	ds_read_b128 v[224:227], v86 offset:224
	ds_read_b128 v[228:231], v86 offset:256
	ds_read_b128 v[232:235], v86 offset:288
	ds_read_b128 v[236:239], v86 offset:320
	ds_read_b128 v[240:243], v86 offset:352
	s_waitcnt lgkmcnt(11)
	v_mfma_f32_32x32x16_bf16 v[82:97], v[82:85], v[142:145], 0
	v_sub_f32_e32 v66, v66, v183
	v_sub_f32_e32 v78, v78, v183
	v_exp_f32_e32 v66, v66
	v_exp_f32_e32 v78, v78
	s_waitcnt lgkmcnt(10)
	v_mfma_f32_32x32x16_bf16 v[82:97], v[188:191], v[138:141], v[82:97]
	v_sub_f32_e32 v67, v67, v183
	v_sub_f32_e32 v79, v79, v183
	v_exp_f32_e32 v67, v67
	v_exp_f32_e32 v79, v79
	v_cvt_pk_bf16_f32 v188, v66, v67
	s_waitcnt lgkmcnt(9)
	v_mfma_f32_32x32x16_bf16 v[82:97], v[192:195], v[134:137], v[82:97]
	v_sub_f32_e32 v68, v68, v183
	v_sub_f32_e32 v80, v80, v183
	v_exp_f32_e32 v68, v68
	v_exp_f32_e32 v80, v80
	s_waitcnt lgkmcnt(8)
	v_mfma_f32_32x32x16_bf16 v[82:97], v[196:199], v[130:133], v[82:97]
	v_sub_f32_e32 v69, v69, v183
	v_sub_f32_e32 v81, v81, v183
	v_exp_f32_e32 v69, v69
	v_exp_f32_e32 v81, v81
	v_cvt_pk_bf16_f32 v194, v78, v79
	v_cvt_pk_bf16_f32 v189, v68, v69
	v_cvt_pk_bf16_f32 v195, v80, v81
	s_waitcnt lgkmcnt(7)
	v_mfma_f32_32x32x16_bf16 v[82:97], v[200:203], v[126:129], v[82:97]
	v_sub_f32_e32 v70, v70, v183
	v_exp_f32_e32 v70, v70
	s_waitcnt lgkmcnt(6)
	v_mfma_f32_32x32x16_bf16 v[82:97], v[216:219], v[122:125], v[82:97]
	v_sub_f32_e32 v71, v71, v183
	v_exp_f32_e32 v71, v71
	s_nop 0
	v_cvt_pk_bf16_f32 v190, v70, v71
	s_waitcnt lgkmcnt(5)
	v_mfma_f32_32x32x16_bf16 v[82:97], v[220:223], v[118:121], v[82:97]
	v_sub_f32_e32 v72, v72, v183
	v_exp_f32_e32 v72, v72
	s_waitcnt lgkmcnt(4)
	v_mfma_f32_32x32x16_bf16 v[82:97], v[224:227], v[114:117], v[82:97]
	v_sub_f32_e32 v73, v73, v183
	v_exp_f32_e32 v73, v73
	s_nop 0
	v_cvt_pk_bf16_f32 v191, v72, v73
	s_waitcnt lgkmcnt(3)
	v_mfma_f32_32x32x16_bf16 v[82:97], v[228:231], v[110:113], v[82:97]
	v_add_u32_e32 v204, s12, v187
	v_sub_f32_e32 v74, v74, v183
	ds_read_b128 v[196:199], v204
	ds_read_b128 v[200:203], v204 offset:32
	v_exp_f32_e32 v74, v74
	s_waitcnt lgkmcnt(4)
	v_mfma_f32_32x32x16_bf16 v[82:97], v[232:235], v[106:109], v[82:97]
	v_sub_f32_e32 v75, v75, v183
	ds_read_b128 v[216:219], v204 offset:4608
	ds_read_b128 v[220:223], v204 offset:4640
	v_exp_f32_e32 v75, v75
	s_nop 0
	v_cvt_pk_bf16_f32 v192, v74, v75
	s_waitcnt lgkmcnt(5)
	v_mfma_f32_32x32x16_bf16 v[82:97], v[236:239], v[102:105], v[82:97]
	v_sub_f32_e32 v76, v76, v183
	ds_read_b128 v[224:227], v204 offset:9216
	ds_read_b128 v[228:231], v204 offset:9248
	v_exp_f32_e32 v76, v76
	s_waitcnt lgkmcnt(6)
	v_mfma_f32_32x32x16_bf16 v[82:97], v[240:243], v[98:101], v[82:97]
	v_sub_f32_e32 v77, v77, v183
	ds_read_b128 v[232:235], v204 offset:13824
	ds_read_b128 v[236:239], v204 offset:13856
	v_exp_f32_e32 v77, v77
	s_nop 0
	v_cvt_pk_bf16_f32 v193, v76, v77
	s_and_b64 vcc, exec, s[0:1]
	s_cbranch_vccnz .LattA_slow
	s_mul_i32 s12, s36, 0x6400
	s_add_u32 s16, s80, s2
	s_addc_u32 s17, s81, s3
	s_add_u32 s16, s16, 0x30e8a000
	s_addc_u32 s17, s17, 0
	s_add_i32 m0, s12, s65
	s_waitcnt lgkmcnt(0)
	v_mfma_f32_32x32x16_bf16 v[50:65], v[196:199], v[188:191], v[50:65]
	global_load_lds_dwordx4 v208, s[16:17]
	s_add_i32 m0, s12, s66
	v_mfma_f32_32x32x16_bf16 v[34:49], v[216:219], v[188:191], v[34:49]
	global_load_lds_dwordx4 v209, s[16:17]
	s_add_i32 m0, s12, s67
	s_add_i32 s12, s12, s68
	v_mfma_f32_32x32x16_bf16 v[18:33], v[224:227], v[188:191], v[18:33]
	v_max_f32_e32 v152, v82, v83
	v_max3_f32 v152, v152, v84, v85
	global_load_lds_dwordx4 v210, s[16:17]
	s_add_i32 m0, s12, 0x6000
	s_mul_i32 s12, s36, 0x4800
	s_add_i32 s13, s12, 0xffffb800
	s_cmp_lg_u32 s36, 0
	v_mfma_f32_32x32x16_bf16 v[2:17], v[232:235], v[188:191], v[2:17]
	v_max3_f32 v152, v152, v86, v87
	v_max3_f32 v152, v152, v88, v89
	global_load_lds_dwordx4 v211, s[16:17]
	s_cselect_b32 s13, s13, 0x9000
	s_add_i32 s13, s13, 0x12c00
	s_add_u32 s16, s82, s2
	s_addc_u32 s17, s83, s3
	s_add_u32 s16, s16, s28
	s_addc_u32 s17, s17, s29
	s_add_i32 m0, s13, s69
	v_mfma_f32_32x32x16_bf16 v[50:65], v[200:203], v[192:195], v[50:65]
	v_max3_f32 v152, v152, v90, v91
	v_max3_f32 v152, v152, v92, v93
	global_load_lds_dwordx4 v212, s[16:17]
	s_add_i32 m0, s13, s70
	v_mfma_f32_32x32x16_bf16 v[34:49], v[220:223], v[192:195], v[34:49]
	v_max3_f32 v152, v152, v94, v95
	v_max3_f32 v152, v152, v96, v97
	global_load_lds_dwordx4 v213, s[16:17]
	s_add_i32 m0, s13, s71
	v_mfma_f32_32x32x16_bf16 v[18:33], v[228:231], v[192:195], v[18:33]
	global_load_lds_dwordx4 v214, s[16:17]
	v_mfma_f32_32x32x16_bf16 v[2:17], v[236:239], v[192:195], v[2:17]
	v_mov_b32_e32 v153, v152
	s_nop 1
	v_permlane32_swap_b32_e32 v153, v152
	v_max_f32_e32 v152, v152, v153
	s_branch .LattA_join
